# plus the in-projection gate epilogue re-emitted with -log2e folded into fma constant, bias and clamp bounds (134 issue slots per group instead of 150)
# speedup vs baseline: 1.0061x; 1.0013x over previous
.LBB0_144:
	s_add_i32 s0, s6, -15
	v_lshl_or_b32 v48, s0, 7, v184
	v_lshlrev_b64 v[0:1], 2, v[48:49]
	v_lshl_add_u64 v[4:5], s[48:49], 0, v[0:1]
	v_lshl_add_u64 v[12:13], s[58:59], 0, v[0:1]
	global_load_dwordx4 v[0:3], v[4:5], off offset:16
	global_load_dwordx4 v[8:11], v[4:5], off
	s_nop 0
	global_load_dwordx4 v[4:7], v[12:13], off offset:16
	s_nop 0
	global_load_dwordx4 v[12:15], v[12:13], off
	s_and_b32 s1, s0, 1
	s_lshl_b32 s0, s0, 2
	s_and_b32 s0, s0, 0xffffff8
	s_add_i32 s0, s8, s0
	s_lshl_b32 s4, s68, 9
	s_lshl_b32 s0, s0, 4
	s_add_i32 s0, s0, s4
	s_or_b32 s70, s0, s1
	s_ashr_i32 s71, s70, 31
	s_lshl_b64 s[0:1], s[70:71], 10
	s_waitcnt vmcnt(0)
	s_mov_b32 s5, 0xc22d1f97
	v_mov_b32_e32 v175, 0x422d1f97
	v_mul_f32_e32 v0, 0xbfb8aa3b, v0
	v_mul_f32_e32 v1, 0xbfb8aa3b, v1
	v_mul_f32_e32 v2, 0xbfb8aa3b, v2
	v_mul_f32_e32 v3, 0xbfb8aa3b, v3
	v_mul_f32_e32 v4, 0xbfb8aa3b, v4
	v_mul_f32_e32 v5, 0xbfb8aa3b, v5
	v_mul_f32_e32 v6, 0xbfb8aa3b, v6
	v_mul_f32_e32 v7, 0xbfb8aa3b, v7
	v_mul_f32_e32 v8, 0xbfb8aa3b, v8
	v_mul_f32_e32 v9, 0xbfb8aa3b, v9
	v_mul_f32_e32 v10, 0xbfb8aa3b, v10
	v_mul_f32_e32 v11, 0xbfb8aa3b, v11
	v_mul_f32_e32 v12, 0xbfb8aa3b, v12
	v_mul_f32_e32 v13, 0xbfb8aa3b, v13
	v_mul_f32_e32 v14, 0xbfb8aa3b, v14
	v_mul_f32_e32 v15, 0xbfb8aa3b, v15
	v_fmamk_f32 v16, v158, 0xbab8aa3b, v8
	v_fmamk_f32 v17, v159, 0xbab8aa3b, v9
	v_fmamk_f32 v18, v160, 0xbab8aa3b, v10
	v_fmamk_f32 v19, v161, 0xbab8aa3b, v11
	v_fmamk_f32 v20, v154, 0xbab8aa3b, v0
	v_fmamk_f32 v21, v155, 0xbab8aa3b, v1
	v_fmamk_f32 v22, v156, 0xbab8aa3b, v2
	v_fmamk_f32 v23, v157, 0xbab8aa3b, v3
	v_fmamk_f32 v24, v150, 0xbab8aa3b, v12
	v_fmamk_f32 v25, v151, 0xbab8aa3b, v13
	v_fmamk_f32 v26, v152, 0xbab8aa3b, v14
	v_fmamk_f32 v27, v153, 0xbab8aa3b, v15
	v_fmamk_f32 v28, v146, 0xbab8aa3b, v4
	v_fmamk_f32 v29, v147, 0xbab8aa3b, v5
	v_fmamk_f32 v30, v148, 0xbab8aa3b, v6
	v_fmamk_f32 v31, v149, 0xbab8aa3b, v7
	v_med3_f32 v16, v16, s5, v175
	v_med3_f32 v17, v17, s5, v175
	v_med3_f32 v18, v18, s5, v175
	v_med3_f32 v19, v19, s5, v175
	v_med3_f32 v20, v20, s5, v175
	v_med3_f32 v21, v21, s5, v175
	v_med3_f32 v22, v22, s5, v175
	v_med3_f32 v23, v23, s5, v175
	v_med3_f32 v24, v24, s5, v175
	v_med3_f32 v25, v25, s5, v175
	v_med3_f32 v26, v26, s5, v175
	v_med3_f32 v27, v27, s5, v175
	v_med3_f32 v28, v28, s5, v175
	v_med3_f32 v29, v29, s5, v175
	v_med3_f32 v30, v30, s5, v175
	v_med3_f32 v31, v31, s5, v175
	v_exp_f32_e32 v16, v16
	v_exp_f32_e32 v17, v17
	v_exp_f32_e32 v18, v18
	v_exp_f32_e32 v19, v19
	v_exp_f32_e32 v20, v20
	v_exp_f32_e32 v21, v21
	v_exp_f32_e32 v22, v22
	v_exp_f32_e32 v23, v23
	v_exp_f32_e32 v24, v24
	v_exp_f32_e32 v25, v25
	v_exp_f32_e32 v26, v26
	v_exp_f32_e32 v27, v27
	v_exp_f32_e32 v28, v28
	v_exp_f32_e32 v29, v29
	v_exp_f32_e32 v30, v30
	v_exp_f32_e32 v31, v31
	v_add_f32_e32 v16, 1.0, v16
	v_add_f32_e32 v17, 1.0, v17
	v_add_f32_e32 v18, 1.0, v18
	v_add_f32_e32 v19, 1.0, v19
	v_add_f32_e32 v20, 1.0, v20
	v_add_f32_e32 v21, 1.0, v21
	v_add_f32_e32 v22, 1.0, v22
	v_add_f32_e32 v23, 1.0, v23
	v_add_f32_e32 v24, 1.0, v24
	v_add_f32_e32 v25, 1.0, v25
	v_add_f32_e32 v26, 1.0, v26
	v_add_f32_e32 v27, 1.0, v27
	v_add_f32_e32 v28, 1.0, v28
	v_add_f32_e32 v29, 1.0, v29
	v_add_f32_e32 v30, 1.0, v30
	v_add_f32_e32 v31, 1.0, v31
	v_rcp_f32_e32 v188, v24
	v_rcp_f32_e32 v189, v25
	v_rcp_f32_e32 v190, v26
	v_rcp_f32_e32 v191, v27
	v_rcp_f32_e32 v192, v28
	v_rcp_f32_e32 v193, v29
	v_rcp_f32_e32 v194, v30
	v_rcp_f32_e32 v195, v31
	v_rcp_f32_e32 v16, v16
	v_rcp_f32_e32 v17, v17
	v_rcp_f32_e32 v18, v18
	v_rcp_f32_e32 v19, v19
	v_rcp_f32_e32 v20, v20
	v_rcp_f32_e32 v21, v21
	v_rcp_f32_e32 v22, v22
	v_rcp_f32_e32 v23, v23
	v_or_b32_e32 v176, s0, v187
	v_mov_b32_e32 v177, s1
	v_mul_f32_e32 v24, v24, v16
	v_mul_f32_e32 v25, v25, v17
	v_mul_f32_e32 v26, v26, v18
	v_mul_f32_e32 v27, v27, v19
	v_mul_f32_e32 v28, v28, v20
	v_mul_f32_e32 v29, v29, v21
	v_mul_f32_e32 v30, v30, v22
	v_mul_f32_e32 v31, v31, v23
	v_lshl_add_u64 v[178:179], s[44:45], 0, v[176:177]
	v_lshl_add_u64 v[176:177], s[46:47], 0, v[176:177]
	v_cvt_pk_bf16_f32 v206, v24, v25
	v_cvt_pk_bf16_f32 v207, v26, v27
	v_cvt_pk_bf16_f32 v208, v28, v29
	v_cvt_pk_bf16_f32 v209, v30, v31
	v_cvt_pk_bf16_f32 v210, v188, v189
	v_cvt_pk_bf16_f32 v211, v190, v191
	v_cvt_pk_bf16_f32 v212, v192, v193
	v_cvt_pk_bf16_f32 v213, v194, v195
	global_store_dwordx4 v[178:179], v[206:209], off nt
	global_store_dwordx4 v[176:177], v[210:213], off nt
	v_fmamk_f32 v16, v142, 0xbab8aa3b, v8
	v_fmamk_f32 v17, v143, 0xbab8aa3b, v9
	v_fmamk_f32 v18, v144, 0xbab8aa3b, v10
	v_fmamk_f32 v19, v145, 0xbab8aa3b, v11
	v_fmamk_f32 v20, v138, 0xbab8aa3b, v0
	v_fmamk_f32 v21, v139, 0xbab8aa3b, v1
	v_fmamk_f32 v22, v140, 0xbab8aa3b, v2
	v_fmamk_f32 v23, v141, 0xbab8aa3b, v3
	v_fmamk_f32 v24, v134, 0xbab8aa3b, v12
	v_fmamk_f32 v25, v135, 0xbab8aa3b, v13
	v_fmamk_f32 v26, v136, 0xbab8aa3b, v14
	v_fmamk_f32 v27, v137, 0xbab8aa3b, v15
	v_fmamk_f32 v28, v130, 0xbab8aa3b, v4
	v_fmamk_f32 v29, v131, 0xbab8aa3b, v5
	v_fmamk_f32 v30, v132, 0xbab8aa3b, v6
	v_fmamk_f32 v31, v133, 0xbab8aa3b, v7
	v_med3_f32 v16, v16, s5, v175
	v_med3_f32 v17, v17, s5, v175
	v_med3_f32 v18, v18, s5, v175
	v_med3_f32 v19, v19, s5, v175
	v_med3_f32 v20, v20, s5, v175
	v_med3_f32 v21, v21, s5, v175
	v_med3_f32 v22, v22, s5, v175
	v_med3_f32 v23, v23, s5, v175
	v_med3_f32 v24, v24, s5, v175
	v_med3_f32 v25, v25, s5, v175
	v_med3_f32 v26, v26, s5, v175
	v_med3_f32 v27, v27, s5, v175
	v_med3_f32 v28, v28, s5, v175
	v_med3_f32 v29, v29, s5, v175
	v_med3_f32 v30, v30, s5, v175
	v_med3_f32 v31, v31, s5, v175
	v_exp_f32_e32 v16, v16
	v_exp_f32_e32 v17, v17
	v_exp_f32_e32 v18, v18
	v_exp_f32_e32 v19, v19
	v_exp_f32_e32 v20, v20
	v_exp_f32_e32 v21, v21
	v_exp_f32_e32 v22, v22
	v_exp_f32_e32 v23, v23
	v_exp_f32_e32 v24, v24
	v_exp_f32_e32 v25, v25
	v_exp_f32_e32 v26, v26
	v_exp_f32_e32 v27, v27
	v_exp_f32_e32 v28, v28
	v_exp_f32_e32 v29, v29
	v_exp_f32_e32 v30, v30
	v_exp_f32_e32 v31, v31
	s_or_b32 s0, s70, 2
	s_ashr_i32 s1, s0, 31
	s_lshl_b64 s[0:1], s[0:1], 10
	v_add_f32_e32 v16, 1.0, v16
	v_add_f32_e32 v17, 1.0, v17
	v_add_f32_e32 v18, 1.0, v18
	v_add_f32_e32 v19, 1.0, v19
	v_add_f32_e32 v20, 1.0, v20
	v_add_f32_e32 v21, 1.0, v21
	v_add_f32_e32 v22, 1.0, v22
	v_add_f32_e32 v23, 1.0, v23
	v_add_f32_e32 v24, 1.0, v24
	v_add_f32_e32 v25, 1.0, v25
	v_add_f32_e32 v26, 1.0, v26
	v_add_f32_e32 v27, 1.0, v27
	v_add_f32_e32 v28, 1.0, v28
	v_add_f32_e32 v29, 1.0, v29
	v_add_f32_e32 v30, 1.0, v30
	v_add_f32_e32 v31, 1.0, v31
	v_rcp_f32_e32 v188, v24
	v_rcp_f32_e32 v189, v25
	v_rcp_f32_e32 v190, v26
	v_rcp_f32_e32 v191, v27
	v_rcp_f32_e32 v192, v28
	v_rcp_f32_e32 v193, v29
	v_rcp_f32_e32 v194, v30
	v_rcp_f32_e32 v195, v31
	v_rcp_f32_e32 v16, v16
	v_rcp_f32_e32 v17, v17
	v_rcp_f32_e32 v18, v18
	v_rcp_f32_e32 v19, v19
	v_rcp_f32_e32 v20, v20
	v_rcp_f32_e32 v21, v21
	v_rcp_f32_e32 v22, v22
	v_rcp_f32_e32 v23, v23
	v_or_b32_e32 v176, s0, v187
	v_mov_b32_e32 v177, s1
	v_mul_f32_e32 v24, v24, v16
	v_mul_f32_e32 v25, v25, v17
	v_mul_f32_e32 v26, v26, v18
	v_mul_f32_e32 v27, v27, v19
	v_mul_f32_e32 v28, v28, v20
	v_mul_f32_e32 v29, v29, v21
	v_mul_f32_e32 v30, v30, v22
	v_mul_f32_e32 v31, v31, v23
	v_lshl_add_u64 v[178:179], s[44:45], 0, v[176:177]
	v_lshl_add_u64 v[176:177], s[46:47], 0, v[176:177]
	v_cvt_pk_bf16_f32 v214, v24, v25
	v_cvt_pk_bf16_f32 v215, v26, v27
	v_cvt_pk_bf16_f32 v216, v28, v29
	v_cvt_pk_bf16_f32 v217, v30, v31
	v_cvt_pk_bf16_f32 v218, v188, v189
	v_cvt_pk_bf16_f32 v219, v190, v191
	v_cvt_pk_bf16_f32 v220, v192, v193
	v_cvt_pk_bf16_f32 v221, v194, v195
	global_store_dwordx4 v[178:179], v[214:217], off nt
	global_store_dwordx4 v[176:177], v[218:221], off nt
	v_fmamk_f32 v16, v126, 0xbab8aa3b, v8
	v_fmamk_f32 v17, v127, 0xbab8aa3b, v9
	v_fmamk_f32 v18, v128, 0xbab8aa3b, v10
	v_fmamk_f32 v19, v129, 0xbab8aa3b, v11
	v_fmamk_f32 v20, v122, 0xbab8aa3b, v0
	v_fmamk_f32 v21, v123, 0xbab8aa3b, v1
	v_fmamk_f32 v22, v124, 0xbab8aa3b, v2
	v_fmamk_f32 v23, v125, 0xbab8aa3b, v3
	v_fmamk_f32 v24, v118, 0xbab8aa3b, v12
	v_fmamk_f32 v25, v119, 0xbab8aa3b, v13
	v_fmamk_f32 v26, v120, 0xbab8aa3b, v14
	v_fmamk_f32 v27, v121, 0xbab8aa3b, v15
	v_fmamk_f32 v28, v114, 0xbab8aa3b, v4
	v_fmamk_f32 v29, v115, 0xbab8aa3b, v5
	v_fmamk_f32 v30, v116, 0xbab8aa3b, v6
	v_fmamk_f32 v31, v117, 0xbab8aa3b, v7
	v_med3_f32 v16, v16, s5, v175
	v_med3_f32 v17, v17, s5, v175
	v_med3_f32 v18, v18, s5, v175
	v_med3_f32 v19, v19, s5, v175
	v_med3_f32 v20, v20, s5, v175
	v_med3_f32 v21, v21, s5, v175
	v_med3_f32 v22, v22, s5, v175
	v_med3_f32 v23, v23, s5, v175
	v_med3_f32 v24, v24, s5, v175
	v_med3_f32 v25, v25, s5, v175
	v_med3_f32 v26, v26, s5, v175
	v_med3_f32 v27, v27, s5, v175
	v_med3_f32 v28, v28, s5, v175
	v_med3_f32 v29, v29, s5, v175
	v_med3_f32 v30, v30, s5, v175
	v_med3_f32 v31, v31, s5, v175
	v_exp_f32_e32 v16, v16
	v_exp_f32_e32 v17, v17
	v_exp_f32_e32 v18, v18
	v_exp_f32_e32 v19, v19
	v_exp_f32_e32 v20, v20
	v_exp_f32_e32 v21, v21
	v_exp_f32_e32 v22, v22
	v_exp_f32_e32 v23, v23
	v_exp_f32_e32 v24, v24
	v_exp_f32_e32 v25, v25
	v_exp_f32_e32 v26, v26
	v_exp_f32_e32 v27, v27
	v_exp_f32_e32 v28, v28
	v_exp_f32_e32 v29, v29
	v_exp_f32_e32 v30, v30
	v_exp_f32_e32 v31, v31
	s_or_b32 s0, s70, 4
	s_ashr_i32 s1, s0, 31
	s_lshl_b64 s[0:1], s[0:1], 10
	v_add_f32_e32 v16, 1.0, v16
	v_add_f32_e32 v17, 1.0, v17
	v_add_f32_e32 v18, 1.0, v18
	v_add_f32_e32 v19, 1.0, v19
	v_add_f32_e32 v20, 1.0, v20
	v_add_f32_e32 v21, 1.0, v21
	v_add_f32_e32 v22, 1.0, v22
	v_add_f32_e32 v23, 1.0, v23
	v_add_f32_e32 v24, 1.0, v24
	v_add_f32_e32 v25, 1.0, v25
	v_add_f32_e32 v26, 1.0, v26
	v_add_f32_e32 v27, 1.0, v27
	v_add_f32_e32 v28, 1.0, v28
	v_add_f32_e32 v29, 1.0, v29
	v_add_f32_e32 v30, 1.0, v30
	v_add_f32_e32 v31, 1.0, v31
	v_rcp_f32_e32 v188, v24
	v_rcp_f32_e32 v189, v25
	v_rcp_f32_e32 v190, v26
	v_rcp_f32_e32 v191, v27
	v_rcp_f32_e32 v192, v28
	v_rcp_f32_e32 v193, v29
	v_rcp_f32_e32 v194, v30
	v_rcp_f32_e32 v195, v31
	v_rcp_f32_e32 v16, v16
	v_rcp_f32_e32 v17, v17
	v_rcp_f32_e32 v18, v18
	v_rcp_f32_e32 v19, v19
	v_rcp_f32_e32 v20, v20
	v_rcp_f32_e32 v21, v21
	v_rcp_f32_e32 v22, v22
	v_rcp_f32_e32 v23, v23
	v_or_b32_e32 v176, s0, v187
	v_mov_b32_e32 v177, s1
	v_mul_f32_e32 v24, v24, v16
	v_mul_f32_e32 v25, v25, v17
	v_mul_f32_e32 v26, v26, v18
	v_mul_f32_e32 v27, v27, v19
	v_mul_f32_e32 v28, v28, v20
	v_mul_f32_e32 v29, v29, v21
	v_mul_f32_e32 v30, v30, v22
	v_mul_f32_e32 v31, v31, v23
	v_lshl_add_u64 v[178:179], s[44:45], 0, v[176:177]
	v_lshl_add_u64 v[176:177], s[46:47], 0, v[176:177]
	v_cvt_pk_bf16_f32 v206, v24, v25
	v_cvt_pk_bf16_f32 v207, v26, v27
	v_cvt_pk_bf16_f32 v208, v28, v29
	v_cvt_pk_bf16_f32 v209, v30, v31
	v_cvt_pk_bf16_f32 v210, v188, v189
	v_cvt_pk_bf16_f32 v211, v190, v191
	v_cvt_pk_bf16_f32 v212, v192, v193
	v_cvt_pk_bf16_f32 v213, v194, v195
	global_store_dwordx4 v[178:179], v[206:209], off nt
	global_store_dwordx4 v[176:177], v[210:213], off nt
	v_fmamk_f32 v16, v110, 0xbab8aa3b, v8
	v_fmamk_f32 v17, v111, 0xbab8aa3b, v9
	v_fmamk_f32 v18, v112, 0xbab8aa3b, v10
	v_fmamk_f32 v19, v113, 0xbab8aa3b, v11
	v_fmamk_f32 v20, v106, 0xbab8aa3b, v0
	v_fmamk_f32 v21, v107, 0xbab8aa3b, v1
	v_fmamk_f32 v22, v108, 0xbab8aa3b, v2
	v_fmamk_f32 v23, v109, 0xbab8aa3b, v3
	v_fmamk_f32 v24, v102, 0xbab8aa3b, v12
	v_fmamk_f32 v25, v103, 0xbab8aa3b, v13
	v_fmamk_f32 v26, v104, 0xbab8aa3b, v14
	v_fmamk_f32 v27, v105, 0xbab8aa3b, v15
	v_fmamk_f32 v28, v98, 0xbab8aa3b, v4
	v_fmamk_f32 v29, v99, 0xbab8aa3b, v5
	v_fmamk_f32 v30, v100, 0xbab8aa3b, v6
	v_fmamk_f32 v31, v101, 0xbab8aa3b, v7
	v_med3_f32 v16, v16, s5, v175
	v_med3_f32 v17, v17, s5, v175
	v_med3_f32 v18, v18, s5, v175
	v_med3_f32 v19, v19, s5, v175
	v_med3_f32 v20, v20, s5, v175
	v_med3_f32 v21, v21, s5, v175
	v_med3_f32 v22, v22, s5, v175
	v_med3_f32 v23, v23, s5, v175
	v_med3_f32 v24, v24, s5, v175
	v_med3_f32 v25, v25, s5, v175
	v_med3_f32 v26, v26, s5, v175
	v_med3_f32 v27, v27, s5, v175
	v_med3_f32 v28, v28, s5, v175
	v_med3_f32 v29, v29, s5, v175
	v_med3_f32 v30, v30, s5, v175
	v_med3_f32 v31, v31, s5, v175
	v_exp_f32_e32 v16, v16
	v_exp_f32_e32 v17, v17
	v_exp_f32_e32 v18, v18
	v_exp_f32_e32 v19, v19
	v_exp_f32_e32 v20, v20
	v_exp_f32_e32 v21, v21
	v_exp_f32_e32 v22, v22
	v_exp_f32_e32 v23, v23
	v_exp_f32_e32 v24, v24
	v_exp_f32_e32 v25, v25
	v_exp_f32_e32 v26, v26
	v_exp_f32_e32 v27, v27
	v_exp_f32_e32 v28, v28
	v_exp_f32_e32 v29, v29
	v_exp_f32_e32 v30, v30
	v_exp_f32_e32 v31, v31
	s_or_b32 s0, s70, 6
	s_ashr_i32 s1, s0, 31
	s_lshl_b64 s[0:1], s[0:1], 10
	v_add_f32_e32 v16, 1.0, v16
	v_add_f32_e32 v17, 1.0, v17
	v_add_f32_e32 v18, 1.0, v18
	v_add_f32_e32 v19, 1.0, v19
	v_add_f32_e32 v20, 1.0, v20
	v_add_f32_e32 v21, 1.0, v21
	v_add_f32_e32 v22, 1.0, v22
	v_add_f32_e32 v23, 1.0, v23
	v_add_f32_e32 v24, 1.0, v24
	v_add_f32_e32 v25, 1.0, v25
	v_add_f32_e32 v26, 1.0, v26
	v_add_f32_e32 v27, 1.0, v27
	v_add_f32_e32 v28, 1.0, v28
	v_add_f32_e32 v29, 1.0, v29
	v_add_f32_e32 v30, 1.0, v30
	v_add_f32_e32 v31, 1.0, v31
	v_rcp_f32_e32 v188, v24
	v_rcp_f32_e32 v189, v25
	v_rcp_f32_e32 v190, v26
	v_rcp_f32_e32 v191, v27
	v_rcp_f32_e32 v192, v28
	v_rcp_f32_e32 v193, v29
	v_rcp_f32_e32 v194, v30
	v_rcp_f32_e32 v195, v31
	v_rcp_f32_e32 v16, v16
	v_rcp_f32_e32 v17, v17
	v_rcp_f32_e32 v18, v18
	v_rcp_f32_e32 v19, v19
	v_rcp_f32_e32 v20, v20
	v_rcp_f32_e32 v21, v21
	v_rcp_f32_e32 v22, v22
	v_rcp_f32_e32 v23, v23
	v_or_b32_e32 v176, s0, v187
	v_mov_b32_e32 v177, s1
	v_mul_f32_e32 v24, v24, v16
	v_mul_f32_e32 v25, v25, v17
	v_mul_f32_e32 v26, v26, v18
	v_mul_f32_e32 v27, v27, v19
	v_mul_f32_e32 v28, v28, v20
	v_mul_f32_e32 v29, v29, v21
	v_mul_f32_e32 v30, v30, v22
	v_mul_f32_e32 v31, v31, v23
	v_lshl_add_u64 v[178:179], s[44:45], 0, v[176:177]
	v_lshl_add_u64 v[176:177], s[46:47], 0, v[176:177]
	v_cvt_pk_bf16_f32 v214, v24, v25
	v_cvt_pk_bf16_f32 v215, v26, v27
	v_cvt_pk_bf16_f32 v216, v28, v29
	v_cvt_pk_bf16_f32 v217, v30, v31
	v_cvt_pk_bf16_f32 v218, v188, v189
	v_cvt_pk_bf16_f32 v219, v190, v191
	v_cvt_pk_bf16_f32 v220, v192, v193
	v_cvt_pk_bf16_f32 v221, v194, v195
	global_store_dwordx4 v[178:179], v[214:217], off nt
	global_store_dwordx4 v[176:177], v[218:221], off nt
	v_fmamk_f32 v16, v94, 0xbab8aa3b, v8
	v_fmamk_f32 v17, v95, 0xbab8aa3b, v9
	v_fmamk_f32 v18, v96, 0xbab8aa3b, v10
	v_fmamk_f32 v19, v97, 0xbab8aa3b, v11
	v_fmamk_f32 v20, v90, 0xbab8aa3b, v0
	v_fmamk_f32 v21, v91, 0xbab8aa3b, v1
	v_fmamk_f32 v22, v92, 0xbab8aa3b, v2
	v_fmamk_f32 v23, v93, 0xbab8aa3b, v3
	v_fmamk_f32 v24, v86, 0xbab8aa3b, v12
	v_fmamk_f32 v25, v87, 0xbab8aa3b, v13
	v_fmamk_f32 v26, v88, 0xbab8aa3b, v14
	v_fmamk_f32 v27, v89, 0xbab8aa3b, v15
	v_fmamk_f32 v28, v82, 0xbab8aa3b, v4
	v_fmamk_f32 v29, v83, 0xbab8aa3b, v5
	v_fmamk_f32 v30, v84, 0xbab8aa3b, v6
	v_fmamk_f32 v31, v85, 0xbab8aa3b, v7
	v_med3_f32 v16, v16, s5, v175
	v_med3_f32 v17, v17, s5, v175
	v_med3_f32 v18, v18, s5, v175
	v_med3_f32 v19, v19, s5, v175
	v_med3_f32 v20, v20, s5, v175
	v_med3_f32 v21, v21, s5, v175
	v_med3_f32 v22, v22, s5, v175
	v_med3_f32 v23, v23, s5, v175
	v_med3_f32 v24, v24, s5, v175
	v_med3_f32 v25, v25, s5, v175
	v_med3_f32 v26, v26, s5, v175
	v_med3_f32 v27, v27, s5, v175
	v_med3_f32 v28, v28, s5, v175
	v_med3_f32 v29, v29, s5, v175
	v_med3_f32 v30, v30, s5, v175
	v_med3_f32 v31, v31, s5, v175
	v_exp_f32_e32 v16, v16
	v_exp_f32_e32 v17, v17
	v_exp_f32_e32 v18, v18
	v_exp_f32_e32 v19, v19
	v_exp_f32_e32 v20, v20
	v_exp_f32_e32 v21, v21
	v_exp_f32_e32 v22, v22
	v_exp_f32_e32 v23, v23
	v_exp_f32_e32 v24, v24
	v_exp_f32_e32 v25, v25
	v_exp_f32_e32 v26, v26
	v_exp_f32_e32 v27, v27
	v_exp_f32_e32 v28, v28
	v_exp_f32_e32 v29, v29
	v_exp_f32_e32 v30, v30
	v_exp_f32_e32 v31, v31
	s_or_b32 s0, s70, 8
	s_ashr_i32 s1, s0, 31
	s_lshl_b64 s[0:1], s[0:1], 10
	v_add_f32_e32 v16, 1.0, v16
	v_add_f32_e32 v17, 1.0, v17
	v_add_f32_e32 v18, 1.0, v18
	v_add_f32_e32 v19, 1.0, v19
	v_add_f32_e32 v20, 1.0, v20
	v_add_f32_e32 v21, 1.0, v21
	v_add_f32_e32 v22, 1.0, v22
	v_add_f32_e32 v23, 1.0, v23
	v_add_f32_e32 v24, 1.0, v24
	v_add_f32_e32 v25, 1.0, v25
	v_add_f32_e32 v26, 1.0, v26
	v_add_f32_e32 v27, 1.0, v27
	v_add_f32_e32 v28, 1.0, v28
	v_add_f32_e32 v29, 1.0, v29
	v_add_f32_e32 v30, 1.0, v30
	v_add_f32_e32 v31, 1.0, v31
	v_rcp_f32_e32 v188, v24
	v_rcp_f32_e32 v189, v25
	v_rcp_f32_e32 v190, v26
	v_rcp_f32_e32 v191, v27
	v_rcp_f32_e32 v192, v28
	v_rcp_f32_e32 v193, v29
	v_rcp_f32_e32 v194, v30
	v_rcp_f32_e32 v195, v31
	v_rcp_f32_e32 v16, v16
	v_rcp_f32_e32 v17, v17
	v_rcp_f32_e32 v18, v18
	v_rcp_f32_e32 v19, v19
	v_rcp_f32_e32 v20, v20
	v_rcp_f32_e32 v21, v21
	v_rcp_f32_e32 v22, v22
	v_rcp_f32_e32 v23, v23
	v_or_b32_e32 v176, s0, v187
	v_mov_b32_e32 v177, s1
	v_mul_f32_e32 v24, v24, v16
	v_mul_f32_e32 v25, v25, v17
	v_mul_f32_e32 v26, v26, v18
	v_mul_f32_e32 v27, v27, v19
	v_mul_f32_e32 v28, v28, v20
	v_mul_f32_e32 v29, v29, v21
	v_mul_f32_e32 v30, v30, v22
	v_mul_f32_e32 v31, v31, v23
	v_lshl_add_u64 v[178:179], s[44:45], 0, v[176:177]
	v_lshl_add_u64 v[176:177], s[46:47], 0, v[176:177]
	v_cvt_pk_bf16_f32 v206, v24, v25
	v_cvt_pk_bf16_f32 v207, v26, v27
	v_cvt_pk_bf16_f32 v208, v28, v29
	v_cvt_pk_bf16_f32 v209, v30, v31
	v_cvt_pk_bf16_f32 v210, v188, v189
	v_cvt_pk_bf16_f32 v211, v190, v191
	v_cvt_pk_bf16_f32 v212, v192, v193
	v_cvt_pk_bf16_f32 v213, v194, v195
	global_store_dwordx4 v[178:179], v[206:209], off nt
	global_store_dwordx4 v[176:177], v[210:213], off nt
	v_fmamk_f32 v16, v70, 0xbab8aa3b, v8
	v_fmamk_f32 v17, v71, 0xbab8aa3b, v9
	v_fmamk_f32 v18, v72, 0xbab8aa3b, v10
	v_fmamk_f32 v19, v73, 0xbab8aa3b, v11
	v_fmamk_f32 v20, v66, 0xbab8aa3b, v0
	v_fmamk_f32 v21, v67, 0xbab8aa3b, v1
	v_fmamk_f32 v22, v68, 0xbab8aa3b, v2
	v_fmamk_f32 v23, v69, 0xbab8aa3b, v3
	v_fmamk_f32 v24, v62, 0xbab8aa3b, v12
	v_fmamk_f32 v25, v63, 0xbab8aa3b, v13
	v_fmamk_f32 v26, v64, 0xbab8aa3b, v14
	v_fmamk_f32 v27, v65, 0xbab8aa3b, v15
	v_fmamk_f32 v28, v50, 0xbab8aa3b, v4
	v_fmamk_f32 v29, v51, 0xbab8aa3b, v5
	v_fmamk_f32 v30, v52, 0xbab8aa3b, v6
	v_fmamk_f32 v31, v53, 0xbab8aa3b, v7
	v_med3_f32 v16, v16, s5, v175
	v_med3_f32 v17, v17, s5, v175
	v_med3_f32 v18, v18, s5, v175
	v_med3_f32 v19, v19, s5, v175
	v_med3_f32 v20, v20, s5, v175
	v_med3_f32 v21, v21, s5, v175
	v_med3_f32 v22, v22, s5, v175
	v_med3_f32 v23, v23, s5, v175
	v_med3_f32 v24, v24, s5, v175
	v_med3_f32 v25, v25, s5, v175
	v_med3_f32 v26, v26, s5, v175
	v_med3_f32 v27, v27, s5, v175
	v_med3_f32 v28, v28, s5, v175
	v_med3_f32 v29, v29, s5, v175
	v_med3_f32 v30, v30, s5, v175
	v_med3_f32 v31, v31, s5, v175
	v_exp_f32_e32 v16, v16
	v_exp_f32_e32 v17, v17
	v_exp_f32_e32 v18, v18
	v_exp_f32_e32 v19, v19
	v_exp_f32_e32 v20, v20
	v_exp_f32_e32 v21, v21
	v_exp_f32_e32 v22, v22
	v_exp_f32_e32 v23, v23
	v_exp_f32_e32 v24, v24
	v_exp_f32_e32 v25, v25
	v_exp_f32_e32 v26, v26
	v_exp_f32_e32 v27, v27
	v_exp_f32_e32 v28, v28
	v_exp_f32_e32 v29, v29
	v_exp_f32_e32 v30, v30
	v_exp_f32_e32 v31, v31
	s_or_b32 s0, s70, 10
	s_ashr_i32 s1, s0, 31
	s_lshl_b64 s[0:1], s[0:1], 10
	v_add_f32_e32 v16, 1.0, v16
	v_add_f32_e32 v17, 1.0, v17
	v_add_f32_e32 v18, 1.0, v18
	v_add_f32_e32 v19, 1.0, v19
	v_add_f32_e32 v20, 1.0, v20
	v_add_f32_e32 v21, 1.0, v21
	v_add_f32_e32 v22, 1.0, v22
	v_add_f32_e32 v23, 1.0, v23
	v_add_f32_e32 v24, 1.0, v24
	v_add_f32_e32 v25, 1.0, v25
	v_add_f32_e32 v26, 1.0, v26
	v_add_f32_e32 v27, 1.0, v27
	v_add_f32_e32 v28, 1.0, v28
	v_add_f32_e32 v29, 1.0, v29
	v_add_f32_e32 v30, 1.0, v30
	v_add_f32_e32 v31, 1.0, v31
	v_rcp_f32_e32 v188, v24
	v_rcp_f32_e32 v189, v25
	v_rcp_f32_e32 v190, v26
	v_rcp_f32_e32 v191, v27
	v_rcp_f32_e32 v192, v28
	v_rcp_f32_e32 v193, v29
	v_rcp_f32_e32 v194, v30
	v_rcp_f32_e32 v195, v31
	v_rcp_f32_e32 v16, v16
	v_rcp_f32_e32 v17, v17
	v_rcp_f32_e32 v18, v18
	v_rcp_f32_e32 v19, v19
	v_rcp_f32_e32 v20, v20
	v_rcp_f32_e32 v21, v21
	v_rcp_f32_e32 v22, v22
	v_rcp_f32_e32 v23, v23
	v_or_b32_e32 v176, s0, v187
	v_mov_b32_e32 v177, s1
	v_mul_f32_e32 v24, v24, v16
	v_mul_f32_e32 v25, v25, v17
	v_mul_f32_e32 v26, v26, v18
	v_mul_f32_e32 v27, v27, v19
	v_mul_f32_e32 v28, v28, v20
	v_mul_f32_e32 v29, v29, v21
	v_mul_f32_e32 v30, v30, v22
	v_mul_f32_e32 v31, v31, v23
	v_lshl_add_u64 v[178:179], s[44:45], 0, v[176:177]
	v_lshl_add_u64 v[176:177], s[46:47], 0, v[176:177]
	v_cvt_pk_bf16_f32 v214, v24, v25
	v_cvt_pk_bf16_f32 v215, v26, v27
	v_cvt_pk_bf16_f32 v216, v28, v29
	v_cvt_pk_bf16_f32 v217, v30, v31
	v_cvt_pk_bf16_f32 v218, v188, v189
	v_cvt_pk_bf16_f32 v219, v190, v191
	v_cvt_pk_bf16_f32 v220, v192, v193
	v_cvt_pk_bf16_f32 v221, v194, v195
	global_store_dwordx4 v[178:179], v[214:217], off nt
	global_store_dwordx4 v[176:177], v[218:221], off nt
	v_fmamk_f32 v16, v44, 0xbab8aa3b, v8
	v_fmamk_f32 v17, v45, 0xbab8aa3b, v9
	v_fmamk_f32 v18, v46, 0xbab8aa3b, v10
	v_fmamk_f32 v19, v47, 0xbab8aa3b, v11
	v_fmamk_f32 v20, v40, 0xbab8aa3b, v0
	v_fmamk_f32 v21, v41, 0xbab8aa3b, v1
	v_fmamk_f32 v22, v42, 0xbab8aa3b, v2
	v_fmamk_f32 v23, v43, 0xbab8aa3b, v3
	v_fmamk_f32 v24, v78, 0xbab8aa3b, v12
	v_fmamk_f32 v25, v79, 0xbab8aa3b, v13
	v_fmamk_f32 v26, v80, 0xbab8aa3b, v14
	v_fmamk_f32 v27, v81, 0xbab8aa3b, v15
	v_fmamk_f32 v28, v74, 0xbab8aa3b, v4
	v_fmamk_f32 v29, v75, 0xbab8aa3b, v5
	v_fmamk_f32 v30, v76, 0xbab8aa3b, v6
	v_fmamk_f32 v31, v77, 0xbab8aa3b, v7
	v_med3_f32 v16, v16, s5, v175
	v_med3_f32 v17, v17, s5, v175
	v_med3_f32 v18, v18, s5, v175
	v_med3_f32 v19, v19, s5, v175
	v_med3_f32 v20, v20, s5, v175
	v_med3_f32 v21, v21, s5, v175
	v_med3_f32 v22, v22, s5, v175
	v_med3_f32 v23, v23, s5, v175
	v_med3_f32 v24, v24, s5, v175
	v_med3_f32 v25, v25, s5, v175
	v_med3_f32 v26, v26, s5, v175
	v_med3_f32 v27, v27, s5, v175
	v_med3_f32 v28, v28, s5, v175
	v_med3_f32 v29, v29, s5, v175
	v_med3_f32 v30, v30, s5, v175
	v_med3_f32 v31, v31, s5, v175
	v_exp_f32_e32 v16, v16
	v_exp_f32_e32 v17, v17
	v_exp_f32_e32 v18, v18
	v_exp_f32_e32 v19, v19
	v_exp_f32_e32 v20, v20
	v_exp_f32_e32 v21, v21
	v_exp_f32_e32 v22, v22
	v_exp_f32_e32 v23, v23
	v_exp_f32_e32 v24, v24
	v_exp_f32_e32 v25, v25
	v_exp_f32_e32 v26, v26
	v_exp_f32_e32 v27, v27
	v_exp_f32_e32 v28, v28
	v_exp_f32_e32 v29, v29
	v_exp_f32_e32 v30, v30
	v_exp_f32_e32 v31, v31
	s_or_b32 s0, s70, 12
	s_ashr_i32 s1, s0, 31
	s_lshl_b64 s[0:1], s[0:1], 10
	v_add_f32_e32 v16, 1.0, v16
	v_add_f32_e32 v17, 1.0, v17
	v_add_f32_e32 v18, 1.0, v18
	v_add_f32_e32 v19, 1.0, v19
	v_add_f32_e32 v20, 1.0, v20
	v_add_f32_e32 v21, 1.0, v21
	v_add_f32_e32 v22, 1.0, v22
	v_add_f32_e32 v23, 1.0, v23
	v_add_f32_e32 v24, 1.0, v24
	v_add_f32_e32 v25, 1.0, v25
	v_add_f32_e32 v26, 1.0, v26
	v_add_f32_e32 v27, 1.0, v27
	v_add_f32_e32 v28, 1.0, v28
	v_add_f32_e32 v29, 1.0, v29
	v_add_f32_e32 v30, 1.0, v30
	v_add_f32_e32 v31, 1.0, v31
	v_rcp_f32_e32 v188, v24
	v_rcp_f32_e32 v189, v25
	v_rcp_f32_e32 v190, v26
	v_rcp_f32_e32 v191, v27
	v_rcp_f32_e32 v192, v28
	v_rcp_f32_e32 v193, v29
	v_rcp_f32_e32 v194, v30
	v_rcp_f32_e32 v195, v31
	v_rcp_f32_e32 v16, v16
	v_rcp_f32_e32 v17, v17
	v_rcp_f32_e32 v18, v18
	v_rcp_f32_e32 v19, v19
	v_rcp_f32_e32 v20, v20
	v_rcp_f32_e32 v21, v21
	v_rcp_f32_e32 v22, v22
	v_rcp_f32_e32 v23, v23
	v_or_b32_e32 v176, s0, v187
	v_mov_b32_e32 v177, s1
	v_mul_f32_e32 v24, v24, v16
	v_mul_f32_e32 v25, v25, v17
	v_mul_f32_e32 v26, v26, v18
	v_mul_f32_e32 v27, v27, v19
	v_mul_f32_e32 v28, v28, v20
	v_mul_f32_e32 v29, v29, v21
	v_mul_f32_e32 v30, v30, v22
	v_mul_f32_e32 v31, v31, v23
	v_lshl_add_u64 v[178:179], s[44:45], 0, v[176:177]
	v_lshl_add_u64 v[176:177], s[46:47], 0, v[176:177]
	v_cvt_pk_bf16_f32 v206, v24, v25
	v_cvt_pk_bf16_f32 v207, v26, v27
	v_cvt_pk_bf16_f32 v208, v28, v29
	v_cvt_pk_bf16_f32 v209, v30, v31
	v_cvt_pk_bf16_f32 v210, v188, v189
	v_cvt_pk_bf16_f32 v211, v190, v191
	v_cvt_pk_bf16_f32 v212, v192, v193
	v_cvt_pk_bf16_f32 v213, v194, v195
	global_store_dwordx4 v[178:179], v[206:209], off nt
	global_store_dwordx4 v[176:177], v[210:213], off nt
	v_fmamk_f32 v16, v36, 0xbab8aa3b, v8
	v_fmamk_f32 v17, v37, 0xbab8aa3b, v9
	v_fmamk_f32 v18, v38, 0xbab8aa3b, v10
	v_fmamk_f32 v19, v39, 0xbab8aa3b, v11
	v_fmamk_f32 v20, v32, 0xbab8aa3b, v0
	v_fmamk_f32 v21, v33, 0xbab8aa3b, v1
	v_fmamk_f32 v22, v34, 0xbab8aa3b, v2
	v_fmamk_f32 v23, v35, 0xbab8aa3b, v3
	v_fmamk_f32 v24, v58, 0xbab8aa3b, v12
	v_fmamk_f32 v25, v59, 0xbab8aa3b, v13
	v_fmamk_f32 v26, v60, 0xbab8aa3b, v14
	v_fmamk_f32 v27, v61, 0xbab8aa3b, v15
	v_fmamk_f32 v28, v54, 0xbab8aa3b, v4
	v_fmamk_f32 v29, v55, 0xbab8aa3b, v5
	v_fmamk_f32 v30, v56, 0xbab8aa3b, v6
	v_fmamk_f32 v31, v57, 0xbab8aa3b, v7
	v_med3_f32 v16, v16, s5, v175
	v_med3_f32 v17, v17, s5, v175
	v_med3_f32 v18, v18, s5, v175
	v_med3_f32 v19, v19, s5, v175
	v_med3_f32 v20, v20, s5, v175
	v_med3_f32 v21, v21, s5, v175
	v_med3_f32 v22, v22, s5, v175
	v_med3_f32 v23, v23, s5, v175
	v_med3_f32 v24, v24, s5, v175
	v_med3_f32 v25, v25, s5, v175
	v_med3_f32 v26, v26, s5, v175
	v_med3_f32 v27, v27, s5, v175
	v_med3_f32 v28, v28, s5, v175
	v_med3_f32 v29, v29, s5, v175
	v_med3_f32 v30, v30, s5, v175
	v_med3_f32 v31, v31, s5, v175
	v_exp_f32_e32 v16, v16
	v_exp_f32_e32 v17, v17
	v_exp_f32_e32 v18, v18
	v_exp_f32_e32 v19, v19
	v_exp_f32_e32 v20, v20
	v_exp_f32_e32 v21, v21
	v_exp_f32_e32 v22, v22
	v_exp_f32_e32 v23, v23
	v_exp_f32_e32 v24, v24
	v_exp_f32_e32 v25, v25
	v_exp_f32_e32 v26, v26
	v_exp_f32_e32 v27, v27
	v_exp_f32_e32 v28, v28
	v_exp_f32_e32 v29, v29
	v_exp_f32_e32 v30, v30
	v_exp_f32_e32 v31, v31
	s_or_b32 s0, s70, 14
	s_ashr_i32 s1, s0, 31
	s_lshl_b64 s[0:1], s[0:1], 10
	v_add_f32_e32 v16, 1.0, v16
	v_add_f32_e32 v17, 1.0, v17
	v_add_f32_e32 v18, 1.0, v18
	v_add_f32_e32 v19, 1.0, v19
	v_add_f32_e32 v20, 1.0, v20
	v_add_f32_e32 v21, 1.0, v21
	v_add_f32_e32 v22, 1.0, v22
	v_add_f32_e32 v23, 1.0, v23
	v_add_f32_e32 v24, 1.0, v24
	v_add_f32_e32 v25, 1.0, v25
	v_add_f32_e32 v26, 1.0, v26
	v_add_f32_e32 v27, 1.0, v27
	v_add_f32_e32 v28, 1.0, v28
	v_add_f32_e32 v29, 1.0, v29
	v_add_f32_e32 v30, 1.0, v30
	v_add_f32_e32 v31, 1.0, v31
	v_rcp_f32_e32 v188, v24
	v_rcp_f32_e32 v189, v25
	v_rcp_f32_e32 v190, v26
	v_rcp_f32_e32 v191, v27
	v_rcp_f32_e32 v192, v28
	v_rcp_f32_e32 v193, v29
	v_rcp_f32_e32 v194, v30
	v_rcp_f32_e32 v195, v31
	v_rcp_f32_e32 v16, v16
	v_rcp_f32_e32 v17, v17
	v_rcp_f32_e32 v18, v18
	v_rcp_f32_e32 v19, v19
	v_rcp_f32_e32 v20, v20
	v_rcp_f32_e32 v21, v21
	v_rcp_f32_e32 v22, v22
	v_rcp_f32_e32 v23, v23
	v_or_b32_e32 v176, s0, v187
	v_mov_b32_e32 v177, s1
	v_mul_f32_e32 v24, v24, v16
	v_mul_f32_e32 v25, v25, v17
	v_mul_f32_e32 v26, v26, v18
	v_mul_f32_e32 v27, v27, v19
	v_mul_f32_e32 v28, v28, v20
	v_mul_f32_e32 v29, v29, v21
	v_mul_f32_e32 v30, v30, v22
	v_mul_f32_e32 v31, v31, v23
	v_lshl_add_u64 v[178:179], s[44:45], 0, v[176:177]
	v_lshl_add_u64 v[176:177], s[46:47], 0, v[176:177]
	v_cvt_pk_bf16_f32 v214, v24, v25
	v_cvt_pk_bf16_f32 v215, v26, v27
	v_cvt_pk_bf16_f32 v216, v28, v29
	v_cvt_pk_bf16_f32 v217, v30, v31
	v_cvt_pk_bf16_f32 v218, v188, v189
	v_cvt_pk_bf16_f32 v219, v190, v191
	v_cvt_pk_bf16_f32 v220, v192, v193
	v_cvt_pk_bf16_f32 v221, v194, v195
	global_store_dwordx4 v[178:179], v[214:217], off nt
	global_store_dwordx4 v[176:177], v[218:221], off nt
	s_cbranch_execnz .LBB0_143
